# speedup vs baseline: 1.0115x; 1.0115x over previous
.LBB3_4:
	s_or_b64 exec, exec, s[2:3]
	s_mov_b32 s24, s8
	s_and_b32 s25, s9, 0xffff
	s_mov_b32 s26, 0x7fffffff
	s_mov_b32 s27, 0x20000
	v_lshlrev_b32_e32 v17, 2, v22
	buffer_load_dword v32, v17, s[24:27], 0 offen
	buffer_load_dword v36, v17, s[24:27], 0 offen offset:16
	buffer_load_dword v40, v17, s[24:27], 0 offen offset:32
	buffer_load_dword v44, v17, s[24:27], 0 offen offset:48
	buffer_load_dword v48, v17, s[24:27], 0 offen offset:64
	buffer_load_dword v52, v17, s[24:27], 0 offen offset:80
	buffer_load_dword v56, v17, s[24:27], 0 offen offset:96
	v_sub_u32_e32 v16, v31, v22
	v_mov_b32_e32 v29, 0x7ffffff0
	v_cmp_lt_i32_e64 s[28:29], 0, v16
	v_cmp_lt_i32_e64 s[30:31], 4, v16
	v_cmp_lt_i32_e64 s[32:33], 8, v16
	v_cmp_lt_i32_e64 s[34:35], 12, v16
	v_cmp_lt_i32_e64 s[36:37], 16, v16
	v_cmp_lt_i32_e64 s[38:39], 20, v16
	v_cmp_lt_i32_e64 s[40:41], 24, v16
	s_waitcnt vmcnt(6)
	v_lshlrev_b32_e32 v23, 4, v32
	v_cndmask_b32_e64 v23, v29, v23, s[28:29]
	buffer_load_dwordx4 v[32:35], v23, s[4:7], 0 offen
	s_waitcnt vmcnt(6)
	v_lshlrev_b32_e32 v23, 4, v36
	v_cndmask_b32_e64 v23, v29, v23, s[30:31]
	buffer_load_dwordx4 v[36:39], v23, s[4:7], 0 offen
	s_waitcnt vmcnt(6)
	v_lshlrev_b32_e32 v23, 4, v40
	v_cndmask_b32_e64 v23, v29, v23, s[32:33]
	buffer_load_dwordx4 v[40:43], v23, s[4:7], 0 offen
	s_waitcnt vmcnt(6)
	v_lshlrev_b32_e32 v23, 4, v44
	v_cndmask_b32_e64 v23, v29, v23, s[34:35]
	buffer_load_dwordx4 v[44:47], v23, s[4:7], 0 offen
	s_waitcnt vmcnt(6)
	v_lshlrev_b32_e32 v23, 4, v48
	v_cndmask_b32_e64 v23, v29, v23, s[36:37]
	buffer_load_dwordx4 v[48:51], v23, s[4:7], 0 offen
	s_waitcnt vmcnt(6)
	v_lshlrev_b32_e32 v23, 4, v52
	v_cndmask_b32_e64 v23, v29, v23, s[38:39]
	buffer_load_dwordx4 v[52:55], v23, s[4:7], 0 offen
	s_waitcnt vmcnt(6)
	v_lshlrev_b32_e32 v23, 4, v56
	v_cndmask_b32_e64 v23, v29, v23, s[40:41]
	buffer_load_dwordx4 v[56:59], v23, s[4:7], 0 offen
	s_waitcnt vmcnt(6)
	v_cvt_pk_f32_fp8_e32 v[24:25], v32
	v_cvt_pk_f32_fp8_sdwa v[60:61], v32 src0_sel:WORD_1
	v_pk_add_f32 v[0:1], v[0:1], v[24:25]
	v_pk_add_f32 v[2:3], v[2:3], v[60:61]
	v_cvt_pk_f32_fp8_e32 v[24:25], v33
	v_cvt_pk_f32_fp8_sdwa v[60:61], v33 src0_sel:WORD_1
	v_pk_add_f32 v[4:5], v[4:5], v[24:25]
	v_pk_add_f32 v[6:7], v[6:7], v[60:61]
	v_cvt_pk_f32_fp8_e32 v[24:25], v34
	v_cvt_pk_f32_fp8_sdwa v[60:61], v34 src0_sel:WORD_1
	v_pk_add_f32 v[8:9], v[8:9], v[24:25]
	v_pk_add_f32 v[10:11], v[10:11], v[60:61]
	v_cvt_pk_f32_fp8_e32 v[24:25], v35
	v_cvt_pk_f32_fp8_sdwa v[60:61], v35 src0_sel:WORD_1
	v_pk_add_f32 v[12:13], v[12:13], v[24:25]
	v_pk_add_f32 v[14:15], v[14:15], v[60:61]
	s_waitcnt vmcnt(5)
	v_cvt_pk_f32_fp8_e32 v[24:25], v36
	v_cvt_pk_f32_fp8_sdwa v[60:61], v36 src0_sel:WORD_1
	v_pk_add_f32 v[0:1], v[0:1], v[24:25]
	v_pk_add_f32 v[2:3], v[2:3], v[60:61]
	v_cvt_pk_f32_fp8_e32 v[24:25], v37
	v_cvt_pk_f32_fp8_sdwa v[60:61], v37 src0_sel:WORD_1
	v_pk_add_f32 v[4:5], v[4:5], v[24:25]
	v_pk_add_f32 v[6:7], v[6:7], v[60:61]
	v_cvt_pk_f32_fp8_e32 v[24:25], v38
	v_cvt_pk_f32_fp8_sdwa v[60:61], v38 src0_sel:WORD_1
	v_pk_add_f32 v[8:9], v[8:9], v[24:25]
	v_pk_add_f32 v[10:11], v[10:11], v[60:61]
	v_cvt_pk_f32_fp8_e32 v[24:25], v39
	v_cvt_pk_f32_fp8_sdwa v[60:61], v39 src0_sel:WORD_1
	v_pk_add_f32 v[12:13], v[12:13], v[24:25]
	v_pk_add_f32 v[14:15], v[14:15], v[60:61]
	s_waitcnt vmcnt(4)
	v_cvt_pk_f32_fp8_e32 v[24:25], v40
	v_cvt_pk_f32_fp8_sdwa v[60:61], v40 src0_sel:WORD_1
	v_pk_add_f32 v[0:1], v[0:1], v[24:25]
	v_pk_add_f32 v[2:3], v[2:3], v[60:61]
	v_cvt_pk_f32_fp8_e32 v[24:25], v41
	v_cvt_pk_f32_fp8_sdwa v[60:61], v41 src0_sel:WORD_1
	v_pk_add_f32 v[4:5], v[4:5], v[24:25]
	v_pk_add_f32 v[6:7], v[6:7], v[60:61]
	v_cvt_pk_f32_fp8_e32 v[24:25], v42
	v_cvt_pk_f32_fp8_sdwa v[60:61], v42 src0_sel:WORD_1
	v_pk_add_f32 v[8:9], v[8:9], v[24:25]
	v_pk_add_f32 v[10:11], v[10:11], v[60:61]
	v_cvt_pk_f32_fp8_e32 v[24:25], v43
	v_cvt_pk_f32_fp8_sdwa v[60:61], v43 src0_sel:WORD_1
	v_pk_add_f32 v[12:13], v[12:13], v[24:25]
	v_pk_add_f32 v[14:15], v[14:15], v[60:61]
	s_waitcnt vmcnt(3)
	v_cvt_pk_f32_fp8_e32 v[24:25], v44
	v_cvt_pk_f32_fp8_sdwa v[60:61], v44 src0_sel:WORD_1
	v_pk_add_f32 v[0:1], v[0:1], v[24:25]
	v_pk_add_f32 v[2:3], v[2:3], v[60:61]
	v_cvt_pk_f32_fp8_e32 v[24:25], v45
	v_cvt_pk_f32_fp8_sdwa v[60:61], v45 src0_sel:WORD_1
	v_pk_add_f32 v[4:5], v[4:5], v[24:25]
	v_pk_add_f32 v[6:7], v[6:7], v[60:61]
	v_cvt_pk_f32_fp8_e32 v[24:25], v46
	v_cvt_pk_f32_fp8_sdwa v[60:61], v46 src0_sel:WORD_1
	v_pk_add_f32 v[8:9], v[8:9], v[24:25]
	v_pk_add_f32 v[10:11], v[10:11], v[60:61]
	v_cvt_pk_f32_fp8_e32 v[24:25], v47
	v_cvt_pk_f32_fp8_sdwa v[60:61], v47 src0_sel:WORD_1
	v_pk_add_f32 v[12:13], v[12:13], v[24:25]
	v_pk_add_f32 v[14:15], v[14:15], v[60:61]
	s_waitcnt vmcnt(2)
	v_cvt_pk_f32_fp8_e32 v[24:25], v48
	v_cvt_pk_f32_fp8_sdwa v[60:61], v48 src0_sel:WORD_1
	v_pk_add_f32 v[0:1], v[0:1], v[24:25]
	v_pk_add_f32 v[2:3], v[2:3], v[60:61]
	v_cvt_pk_f32_fp8_e32 v[24:25], v49
	v_cvt_pk_f32_fp8_sdwa v[60:61], v49 src0_sel:WORD_1
	v_pk_add_f32 v[4:5], v[4:5], v[24:25]
	v_pk_add_f32 v[6:7], v[6:7], v[60:61]
	v_cvt_pk_f32_fp8_e32 v[24:25], v50
	v_cvt_pk_f32_fp8_sdwa v[60:61], v50 src0_sel:WORD_1
	v_pk_add_f32 v[8:9], v[8:9], v[24:25]
	v_pk_add_f32 v[10:11], v[10:11], v[60:61]
	v_cvt_pk_f32_fp8_e32 v[24:25], v51
	v_cvt_pk_f32_fp8_sdwa v[60:61], v51 src0_sel:WORD_1
	v_pk_add_f32 v[12:13], v[12:13], v[24:25]
	v_pk_add_f32 v[14:15], v[14:15], v[60:61]
	s_waitcnt vmcnt(1)
	v_cvt_pk_f32_fp8_e32 v[24:25], v52
	v_cvt_pk_f32_fp8_sdwa v[60:61], v52 src0_sel:WORD_1
	v_pk_add_f32 v[0:1], v[0:1], v[24:25]
	v_pk_add_f32 v[2:3], v[2:3], v[60:61]
	v_cvt_pk_f32_fp8_e32 v[24:25], v53
	v_cvt_pk_f32_fp8_sdwa v[60:61], v53 src0_sel:WORD_1
	v_pk_add_f32 v[4:5], v[4:5], v[24:25]
	v_pk_add_f32 v[6:7], v[6:7], v[60:61]
	v_cvt_pk_f32_fp8_e32 v[24:25], v54
	v_cvt_pk_f32_fp8_sdwa v[60:61], v54 src0_sel:WORD_1
	v_pk_add_f32 v[8:9], v[8:9], v[24:25]
	v_pk_add_f32 v[10:11], v[10:11], v[60:61]
	v_cvt_pk_f32_fp8_e32 v[24:25], v55
	v_cvt_pk_f32_fp8_sdwa v[60:61], v55 src0_sel:WORD_1
	v_pk_add_f32 v[12:13], v[12:13], v[24:25]
	v_pk_add_f32 v[14:15], v[14:15], v[60:61]
	s_waitcnt vmcnt(0)
	v_cvt_pk_f32_fp8_e32 v[24:25], v56
	v_cvt_pk_f32_fp8_sdwa v[60:61], v56 src0_sel:WORD_1
	v_pk_add_f32 v[0:1], v[0:1], v[24:25]
	v_pk_add_f32 v[2:3], v[2:3], v[60:61]
	v_cvt_pk_f32_fp8_e32 v[24:25], v57
	v_cvt_pk_f32_fp8_sdwa v[60:61], v57 src0_sel:WORD_1
	v_pk_add_f32 v[4:5], v[4:5], v[24:25]
	v_pk_add_f32 v[6:7], v[6:7], v[60:61]
	v_cvt_pk_f32_fp8_e32 v[24:25], v58
	v_cvt_pk_f32_fp8_sdwa v[60:61], v58 src0_sel:WORD_1
	v_pk_add_f32 v[8:9], v[8:9], v[24:25]
	v_pk_add_f32 v[10:11], v[10:11], v[60:61]
	v_cvt_pk_f32_fp8_e32 v[24:25], v59
	v_cvt_pk_f32_fp8_sdwa v[60:61], v59 src0_sel:WORD_1
	v_pk_add_f32 v[12:13], v[12:13], v[24:25]
	v_pk_add_f32 v[14:15], v[14:15], v[60:61]
.LBB3_6:
	s_mov_b64 exec, -1
	v_cmp_eq_u32_e64 s[0:1], 0, v28
	s_and_saveexec_b64 s[2:3], s[0:1]
	s_cbranch_execz .LBB3_8

.LBB3_10:
	s_endpgm
	.p2align	8

	.amdhsa_kernel _Z5k_aggILi1EEvPKiS1_S1_PKDv4_jPKfS6_PS2_PDF16_
		.amdhsa_group_segment_fixed_size 0
		.amdhsa_private_segment_fixed_size 0
		.amdhsa_kernarg_size 64
		.amdhsa_user_sgpr_count 2
		.amdhsa_user_sgpr_dispatch_ptr 0
		.amdhsa_user_sgpr_queue_ptr 0
		.amdhsa_user_sgpr_kernarg_segment_ptr 1
		.amdhsa_user_sgpr_dispatch_id 0
		.amdhsa_user_sgpr_kernarg_preload_length 0
		.amdhsa_user_sgpr_kernarg_preload_offset 0
		.amdhsa_user_sgpr_private_segment_size 0
		.amdhsa_uses_dynamic_stack 0
		.amdhsa_enable_private_segment 0
		.amdhsa_system_sgpr_workgroup_id_x 1
		.amdhsa_system_sgpr_workgroup_id_y 0
		.amdhsa_system_sgpr_workgroup_id_z 0
		.amdhsa_system_sgpr_workgroup_info 0
		.amdhsa_system_vgpr_workitem_id 0
		.amdhsa_next_free_vgpr 64
		.amdhsa_next_free_sgpr 42
		.amdhsa_accum_offset 64
		.amdhsa_reserve_vcc 1
		.amdhsa_float_round_mode_32 0
		.amdhsa_float_round_mode_16_64 0
		.amdhsa_float_denorm_mode_32 3
		.amdhsa_float_denorm_mode_16_64 3
		.amdhsa_dx10_clamp 1
		.amdhsa_ieee_mode 1
		.amdhsa_fp16_overflow 0
		.amdhsa_tg_split 0
		.amdhsa_exception_fp_ieee_invalid_op 0
		.amdhsa_exception_fp_denorm_src 0
		.amdhsa_exception_fp_ieee_div_zero 0
		.amdhsa_exception_fp_ieee_overflow 0
		.amdhsa_exception_fp_ieee_underflow 0
		.amdhsa_exception_fp_ieee_inexact 0
		.amdhsa_exception_int_div_zero 0
	.end_amdhsa_kernel

.LBB4_4:
	s_or_b64 exec, exec, s[12:13]
	s_load_dwordx2 s[12:13], s[0:1], 0x38
	s_mov_b32 s24, s8
	s_and_b32 s25, s9, 0xffff
	s_mov_b32 s26, 0x7fffffff
	s_mov_b32 s27, 0x20000
	v_lshlrev_b32_e32 v17, 2, v22
	buffer_load_dword v36, v17, s[24:27], 0 offen
	buffer_load_dword v40, v17, s[24:27], 0 offen offset:16
	buffer_load_dword v44, v17, s[24:27], 0 offen offset:32
	buffer_load_dword v48, v17, s[24:27], 0 offen offset:48
	buffer_load_dword v52, v17, s[24:27], 0 offen offset:64
	buffer_load_dword v56, v17, s[24:27], 0 offen offset:80
	buffer_load_dword v60, v17, s[24:27], 0 offen offset:96
	v_sub_u32_e32 v16, v30, v22
	v_mov_b32_e32 v29, 0x7ffffff0
	v_cmp_lt_i32_e64 s[28:29], 0, v16
	v_cmp_lt_i32_e64 s[30:31], 4, v16
	v_cmp_lt_i32_e64 s[32:33], 8, v16
	v_cmp_lt_i32_e64 s[34:35], 12, v16
	v_cmp_lt_i32_e64 s[36:37], 16, v16
	v_cmp_lt_i32_e64 s[38:39], 20, v16
	v_cmp_lt_i32_e64 s[40:41], 24, v16
	s_waitcnt vmcnt(6)
	v_lshlrev_b32_e32 v23, 4, v36
	v_cndmask_b32_e64 v23, v29, v23, s[28:29]
	buffer_load_dwordx4 v[36:39], v23, s[4:7], 0 offen
	s_waitcnt vmcnt(6)
	v_lshlrev_b32_e32 v23, 4, v40
	v_cndmask_b32_e64 v23, v29, v23, s[30:31]
	buffer_load_dwordx4 v[40:43], v23, s[4:7], 0 offen
	s_waitcnt vmcnt(6)
	v_lshlrev_b32_e32 v23, 4, v44
	v_cndmask_b32_e64 v23, v29, v23, s[32:33]
	buffer_load_dwordx4 v[44:47], v23, s[4:7], 0 offen
	s_waitcnt vmcnt(6)
	v_lshlrev_b32_e32 v23, 4, v48
	v_cndmask_b32_e64 v23, v29, v23, s[34:35]
	buffer_load_dwordx4 v[48:51], v23, s[4:7], 0 offen
	s_waitcnt vmcnt(6)
	v_lshlrev_b32_e32 v23, 4, v52
	v_cndmask_b32_e64 v23, v29, v23, s[36:37]
	buffer_load_dwordx4 v[52:55], v23, s[4:7], 0 offen
	s_waitcnt vmcnt(6)
	v_lshlrev_b32_e32 v23, 4, v56
	v_cndmask_b32_e64 v23, v29, v23, s[38:39]
	buffer_load_dwordx4 v[56:59], v23, s[4:7], 0 offen
	s_waitcnt vmcnt(6)
	v_lshlrev_b32_e32 v23, 4, v60
	v_cndmask_b32_e64 v23, v29, v23, s[40:41]
	buffer_load_dwordx4 v[60:63], v23, s[4:7], 0 offen
	s_waitcnt vmcnt(6)
	v_cvt_pk_f32_fp8_e32 v[24:25], v36
	v_cvt_pk_f32_fp8_sdwa v[32:33], v36 src0_sel:WORD_1
	v_pk_add_f32 v[0:1], v[0:1], v[24:25]
	v_pk_add_f32 v[2:3], v[2:3], v[32:33]
	v_cvt_pk_f32_fp8_e32 v[24:25], v37
	v_cvt_pk_f32_fp8_sdwa v[32:33], v37 src0_sel:WORD_1
	v_pk_add_f32 v[4:5], v[4:5], v[24:25]
	v_pk_add_f32 v[6:7], v[6:7], v[32:33]
	v_cvt_pk_f32_fp8_e32 v[24:25], v38
	v_cvt_pk_f32_fp8_sdwa v[32:33], v38 src0_sel:WORD_1
	v_pk_add_f32 v[8:9], v[8:9], v[24:25]
	v_pk_add_f32 v[10:11], v[10:11], v[32:33]
	v_cvt_pk_f32_fp8_e32 v[24:25], v39
	v_cvt_pk_f32_fp8_sdwa v[32:33], v39 src0_sel:WORD_1
	v_pk_add_f32 v[12:13], v[12:13], v[24:25]
	v_pk_add_f32 v[14:15], v[14:15], v[32:33]
	s_waitcnt vmcnt(5)
	v_cvt_pk_f32_fp8_e32 v[24:25], v40
	v_cvt_pk_f32_fp8_sdwa v[32:33], v40 src0_sel:WORD_1
	v_pk_add_f32 v[0:1], v[0:1], v[24:25]
	v_pk_add_f32 v[2:3], v[2:3], v[32:33]
	v_cvt_pk_f32_fp8_e32 v[24:25], v41
	v_cvt_pk_f32_fp8_sdwa v[32:33], v41 src0_sel:WORD_1
	v_pk_add_f32 v[4:5], v[4:5], v[24:25]
	v_pk_add_f32 v[6:7], v[6:7], v[32:33]
	v_cvt_pk_f32_fp8_e32 v[24:25], v42
	v_cvt_pk_f32_fp8_sdwa v[32:33], v42 src0_sel:WORD_1
	v_pk_add_f32 v[8:9], v[8:9], v[24:25]
	v_pk_add_f32 v[10:11], v[10:11], v[32:33]
	v_cvt_pk_f32_fp8_e32 v[24:25], v43
	v_cvt_pk_f32_fp8_sdwa v[32:33], v43 src0_sel:WORD_1
	v_pk_add_f32 v[12:13], v[12:13], v[24:25]
	v_pk_add_f32 v[14:15], v[14:15], v[32:33]
	s_waitcnt vmcnt(4)
	v_cvt_pk_f32_fp8_e32 v[24:25], v44
	v_cvt_pk_f32_fp8_sdwa v[32:33], v44 src0_sel:WORD_1
	v_pk_add_f32 v[0:1], v[0:1], v[24:25]
	v_pk_add_f32 v[2:3], v[2:3], v[32:33]
	v_cvt_pk_f32_fp8_e32 v[24:25], v45
	v_cvt_pk_f32_fp8_sdwa v[32:33], v45 src0_sel:WORD_1
	v_pk_add_f32 v[4:5], v[4:5], v[24:25]
	v_pk_add_f32 v[6:7], v[6:7], v[32:33]
	v_cvt_pk_f32_fp8_e32 v[24:25], v46
	v_cvt_pk_f32_fp8_sdwa v[32:33], v46 src0_sel:WORD_1
	v_pk_add_f32 v[8:9], v[8:9], v[24:25]
	v_pk_add_f32 v[10:11], v[10:11], v[32:33]
	v_cvt_pk_f32_fp8_e32 v[24:25], v47
	v_cvt_pk_f32_fp8_sdwa v[32:33], v47 src0_sel:WORD_1
	v_pk_add_f32 v[12:13], v[12:13], v[24:25]
	v_pk_add_f32 v[14:15], v[14:15], v[32:33]
	s_waitcnt vmcnt(3)
	v_cvt_pk_f32_fp8_e32 v[24:25], v48
	v_cvt_pk_f32_fp8_sdwa v[32:33], v48 src0_sel:WORD_1
	v_pk_add_f32 v[0:1], v[0:1], v[24:25]
	v_pk_add_f32 v[2:3], v[2:3], v[32:33]
	v_cvt_pk_f32_fp8_e32 v[24:25], v49
	v_cvt_pk_f32_fp8_sdwa v[32:33], v49 src0_sel:WORD_1
	v_pk_add_f32 v[4:5], v[4:5], v[24:25]
	v_pk_add_f32 v[6:7], v[6:7], v[32:33]
	v_cvt_pk_f32_fp8_e32 v[24:25], v50
	v_cvt_pk_f32_fp8_sdwa v[32:33], v50 src0_sel:WORD_1
	v_pk_add_f32 v[8:9], v[8:9], v[24:25]
	v_pk_add_f32 v[10:11], v[10:11], v[32:33]
	v_cvt_pk_f32_fp8_e32 v[24:25], v51
	v_cvt_pk_f32_fp8_sdwa v[32:33], v51 src0_sel:WORD_1
	v_pk_add_f32 v[12:13], v[12:13], v[24:25]
	v_pk_add_f32 v[14:15], v[14:15], v[32:33]
	s_waitcnt vmcnt(2)
	v_cvt_pk_f32_fp8_e32 v[24:25], v52
	v_cvt_pk_f32_fp8_sdwa v[32:33], v52 src0_sel:WORD_1
	v_pk_add_f32 v[0:1], v[0:1], v[24:25]
	v_pk_add_f32 v[2:3], v[2:3], v[32:33]
	v_cvt_pk_f32_fp8_e32 v[24:25], v53
	v_cvt_pk_f32_fp8_sdwa v[32:33], v53 src0_sel:WORD_1
	v_pk_add_f32 v[4:5], v[4:5], v[24:25]
	v_pk_add_f32 v[6:7], v[6:7], v[32:33]
	v_cvt_pk_f32_fp8_e32 v[24:25], v54
	v_cvt_pk_f32_fp8_sdwa v[32:33], v54 src0_sel:WORD_1
	v_pk_add_f32 v[8:9], v[8:9], v[24:25]
	v_pk_add_f32 v[10:11], v[10:11], v[32:33]
	v_cvt_pk_f32_fp8_e32 v[24:25], v55
	v_cvt_pk_f32_fp8_sdwa v[32:33], v55 src0_sel:WORD_1
	v_pk_add_f32 v[12:13], v[12:13], v[24:25]
	v_pk_add_f32 v[14:15], v[14:15], v[32:33]
	s_waitcnt vmcnt(1)
	v_cvt_pk_f32_fp8_e32 v[24:25], v56
	v_cvt_pk_f32_fp8_sdwa v[32:33], v56 src0_sel:WORD_1
	v_pk_add_f32 v[0:1], v[0:1], v[24:25]
	v_pk_add_f32 v[2:3], v[2:3], v[32:33]
	v_cvt_pk_f32_fp8_e32 v[24:25], v57
	v_cvt_pk_f32_fp8_sdwa v[32:33], v57 src0_sel:WORD_1
	v_pk_add_f32 v[4:5], v[4:5], v[24:25]
	v_pk_add_f32 v[6:7], v[6:7], v[32:33]
	v_cvt_pk_f32_fp8_e32 v[24:25], v58
	v_cvt_pk_f32_fp8_sdwa v[32:33], v58 src0_sel:WORD_1
	v_pk_add_f32 v[8:9], v[8:9], v[24:25]
	v_pk_add_f32 v[10:11], v[10:11], v[32:33]
	v_cvt_pk_f32_fp8_e32 v[24:25], v59
	v_cvt_pk_f32_fp8_sdwa v[32:33], v59 src0_sel:WORD_1
	v_pk_add_f32 v[12:13], v[12:13], v[24:25]
	v_pk_add_f32 v[14:15], v[14:15], v[32:33]
	s_waitcnt vmcnt(0)
	v_cvt_pk_f32_fp8_e32 v[24:25], v60
	v_cvt_pk_f32_fp8_sdwa v[32:33], v60 src0_sel:WORD_1
	v_pk_add_f32 v[0:1], v[0:1], v[24:25]
	v_pk_add_f32 v[2:3], v[2:3], v[32:33]
	v_cvt_pk_f32_fp8_e32 v[24:25], v61
	v_cvt_pk_f32_fp8_sdwa v[32:33], v61 src0_sel:WORD_1
	v_pk_add_f32 v[4:5], v[4:5], v[24:25]
	v_pk_add_f32 v[6:7], v[6:7], v[32:33]
	v_cvt_pk_f32_fp8_e32 v[24:25], v62
	v_cvt_pk_f32_fp8_sdwa v[32:33], v62 src0_sel:WORD_1
	v_pk_add_f32 v[8:9], v[8:9], v[24:25]
	v_pk_add_f32 v[10:11], v[10:11], v[32:33]
	v_cvt_pk_f32_fp8_e32 v[24:25], v63
	v_cvt_pk_f32_fp8_sdwa v[32:33], v63 src0_sel:WORD_1
	v_pk_add_f32 v[12:13], v[12:13], v[24:25]
	v_pk_add_f32 v[14:15], v[14:15], v[32:33]

	.amdhsa_kernel _Z5k_aggILi2EEvPKiS1_S1_PKDv4_jPKfS6_PS2_PDF16_
		.amdhsa_group_segment_fixed_size 0
		.amdhsa_private_segment_fixed_size 0
		.amdhsa_kernarg_size 64
		.amdhsa_user_sgpr_count 2
		.amdhsa_user_sgpr_dispatch_ptr 0
		.amdhsa_user_sgpr_queue_ptr 0
		.amdhsa_user_sgpr_kernarg_segment_ptr 1
		.amdhsa_user_sgpr_dispatch_id 0
		.amdhsa_user_sgpr_kernarg_preload_length 0
		.amdhsa_user_sgpr_kernarg_preload_offset 0
		.amdhsa_user_sgpr_private_segment_size 0
		.amdhsa_uses_dynamic_stack 0
		.amdhsa_enable_private_segment 0
		.amdhsa_system_sgpr_workgroup_id_x 1
		.amdhsa_system_sgpr_workgroup_id_y 0
		.amdhsa_system_sgpr_workgroup_id_z 0
		.amdhsa_system_sgpr_workgroup_info 0
		.amdhsa_system_vgpr_workitem_id 0
		.amdhsa_next_free_vgpr 64
		.amdhsa_next_free_sgpr 42
		.amdhsa_accum_offset 64
		.amdhsa_reserve_vcc 1
		.amdhsa_float_round_mode_32 0
		.amdhsa_float_round_mode_16_64 0
		.amdhsa_float_denorm_mode_32 3
		.amdhsa_float_denorm_mode_16_64 3
		.amdhsa_dx10_clamp 1
		.amdhsa_ieee_mode 1
		.amdhsa_fp16_overflow 0
		.amdhsa_tg_split 0
		.amdhsa_exception_fp_ieee_invalid_op 0
		.amdhsa_exception_fp_denorm_src 0
		.amdhsa_exception_fp_ieee_div_zero 0
		.amdhsa_exception_fp_ieee_overflow 0
		.amdhsa_exception_fp_ieee_underflow 0
		.amdhsa_exception_fp_ieee_inexact 0
		.amdhsa_exception_int_div_zero 0
	.end_amdhsa_kernel

	.text
	.p2alignl 8, 3212836864
	.fill 256, 4, 3212836864

amdhsa.kernels:
  - .agpr_count:     0
    .args:
      - .actual_access:  read_only
        .address_space:  global
        .offset:         0
        .size:           8
        .value_kind:     global_buffer
      - .actual_access:  read_only
        .address_space:  global
        .offset:         8
        .size:           8
        .value_kind:     global_buffer
      - .actual_access:  write_only
        .address_space:  global
        .offset:         16
        .size:           8
        .value_kind:     global_buffer
      - .actual_access:  read_only
        .address_space:  global
        .offset:         24
        .size:           8
        .value_kind:     global_buffer
      - .actual_access:  write_only
        .address_space:  global
        .offset:         32
        .size:           8
        .value_kind:     global_buffer
      - .actual_access:  write_only
        .address_space:  global
        .offset:         40
        .size:           8
        .value_kind:     global_buffer
      - .actual_access:  read_only
        .address_space:  global
        .offset:         48
        .size:           8
        .value_kind:     global_buffer
      - .actual_access:  read_only
        .address_space:  global
        .offset:         56
        .size:           8
        .value_kind:     global_buffer
      - .actual_access:  write_only
        .address_space:  global
        .offset:         64
        .size:           8
        .value_kind:     global_buffer
    .group_segment_fixed_size: 53904
    .kernarg_segment_align: 8
    .kernarg_segment_size: 72
    .language:       OpenCL C
    .language_version:
      - 2
      - 0
    .max_flat_workgroup_size: 1024
    .name:           _Z6k_partPKiS0_PiS1_PjS1_PKfS4_Pf
    .private_segment_fixed_size: 0
    .sgpr_count:     31
    .sgpr_spill_count: 0
    .symbol:         _Z6k_partPKiS0_PiS1_PjS1_PKfS4_Pf.kd
    .uniform_work_group_size: 1
    .uses_dynamic_stack: false
    .vgpr_count:     64
    .vgpr_spill_count: 0
    .wavefront_size: 64
  - .agpr_count:     0
    .args:
      - .actual_access:  read_only
        .address_space:  global
        .offset:         0
        .size:           8
        .value_kind:     global_buffer
      - .actual_access:  read_only
        .address_space:  global
        .offset:         8
        .size:           8
        .value_kind:     global_buffer
      - .actual_access:  read_only
        .address_space:  global
        .offset:         16
        .size:           8
        .value_kind:     global_buffer
      - .address_space:  global
        .offset:         24
        .size:           8
        .value_kind:     global_buffer
      - .actual_access:  read_only
        .address_space:  global
        .offset:         32
        .size:           8
        .value_kind:     global_buffer
      - .actual_access:  write_only
        .address_space:  global
        .offset:         40
        .size:           8
        .value_kind:     global_buffer
      - .actual_access:  write_only
        .address_space:  global
        .offset:         48
        .size:           8
        .value_kind:     global_buffer
      - .actual_access:  write_only
        .address_space:  global
        .offset:         56
        .size:           8
        .value_kind:     global_buffer
      - .actual_access:  write_only
        .address_space:  global
        .offset:         64
        .size:           8
        .value_kind:     global_buffer
      - .actual_access:  write_only
        .address_space:  global
        .offset:         72
        .size:           8
        .value_kind:     global_buffer
      - .actual_access:  read_only
        .address_space:  global
        .offset:         80
        .size:           8
        .value_kind:     global_buffer
      - .actual_access:  read_only
        .address_space:  global
        .offset:         88
        .size:           8
        .value_kind:     global_buffer
      - .actual_access:  read_only
        .address_space:  global
        .offset:         96
        .size:           8
        .value_kind:     global_buffer
      - .actual_access:  read_only
        .address_space:  global
        .offset:         104
        .size:           8
        .value_kind:     global_buffer
      - .actual_access:  write_only
        .address_space:  global
        .offset:         112
        .size:           8
        .value_kind:     global_buffer
      - .actual_access:  write_only
        .address_space:  global
        .offset:         120
        .size:           8
        .value_kind:     global_buffer
    .group_segment_fixed_size: 38940
    .kernarg_segment_align: 8
    .kernarg_segment_size: 128
    .language:       OpenCL C
    .language_version:
      - 2
      - 0
    .max_flat_workgroup_size: 1024
    .name:           _Z5k_csrPKjPKiS2_PiPKfPfPDF16_S3_S3_S3_S5_S5_S5_S5_S7_S6_
    .private_segment_fixed_size: 0
    .sgpr_count:     70
    .sgpr_spill_count: 0
    .symbol:         _Z5k_csrPKjPKiS2_PiPKfPfPDF16_S3_S3_S3_S5_S5_S5_S5_S7_S6_.kd
    .uniform_work_group_size: 1
    .uses_dynamic_stack: false
    .vgpr_count:     64
    .vgpr_spill_count: 0
    .wavefront_size: 64
  - .agpr_count:     0
    .args:
      - .actual_access:  read_only
        .address_space:  global
        .offset:         0
        .size:           8
        .value_kind:     global_buffer
      - .actual_access:  read_only
        .address_space:  global
        .offset:         8
        .size:           8
        .value_kind:     global_buffer
      - .actual_access:  read_only
        .address_space:  global
        .offset:         16
        .size:           8
        .value_kind:     global_buffer
      - .actual_access:  read_only
        .address_space:  global
        .offset:         24
        .size:           8
        .value_kind:     global_buffer
      - .actual_access:  read_only
        .address_space:  global
        .offset:         32
        .size:           8
        .value_kind:     global_buffer
      - .actual_access:  read_only
        .address_space:  global
        .offset:         40
        .size:           8
        .value_kind:     global_buffer
      - .actual_access:  write_only
        .address_space:  global
        .offset:         48
        .size:           8
        .value_kind:     global_buffer
      - .offset:         56
        .size:           4
        .value_kind:     hidden_block_count_x
      - .offset:         60
        .size:           4
        .value_kind:     hidden_block_count_y
      - .offset:         64
        .size:           4
        .value_kind:     hidden_block_count_z
      - .offset:         68
        .size:           2
        .value_kind:     hidden_group_size_x
      - .offset:         70
        .size:           2
        .value_kind:     hidden_group_size_y
      - .offset:         72
        .size:           2
        .value_kind:     hidden_group_size_z
      - .offset:         74
        .size:           2
        .value_kind:     hidden_remainder_x
      - .offset:         76
        .size:           2
        .value_kind:     hidden_remainder_y
      - .offset:         78
        .size:           2
        .value_kind:     hidden_remainder_z
      - .offset:         96
        .size:           8
        .value_kind:     hidden_global_offset_x
      - .offset:         104
        .size:           8
        .value_kind:     hidden_global_offset_y
      - .offset:         112
        .size:           8
        .value_kind:     hidden_global_offset_z
      - .offset:         120
        .size:           2
        .value_kind:     hidden_grid_dims
    .group_segment_fixed_size: 32768
    .kernarg_segment_align: 8
    .kernarg_segment_size: 312
    .language:       OpenCL C
    .language_version:
      - 2
      - 0
    .max_flat_workgroup_size: 256
    .name:           _Z5k_decPKiPKDF16_S2_PKfS4_S4_Pf
    .private_segment_fixed_size: 0
    .sgpr_count:     28
    .sgpr_spill_count: 0
    .symbol:         _Z5k_decPKiPKDF16_S2_PKfS4_S4_Pf.kd
    .uniform_work_group_size: 1
    .uses_dynamic_stack: false
    .vgpr_count:     199
    .vgpr_spill_count: 0
    .wavefront_size: 64
  - .agpr_count:     0
    .args:
      - .actual_access:  read_only
        .address_space:  global
        .offset:         0
        .size:           8
        .value_kind:     global_buffer
      - .actual_access:  read_only
        .address_space:  global
        .offset:         8
        .size:           8
        .value_kind:     global_buffer
      - .actual_access:  read_only
        .address_space:  global
        .offset:         16
        .size:           8
        .value_kind:     global_buffer
      - .actual_access:  read_only
        .address_space:  global
        .offset:         24
        .size:           8
        .value_kind:     global_buffer
      - .actual_access:  read_only
        .address_space:  global
        .offset:         32
        .size:           8
        .value_kind:     global_buffer
      - .actual_access:  read_only
        .address_space:  global
        .offset:         40
        .size:           8
        .value_kind:     global_buffer
      - .actual_access:  write_only
        .address_space:  global
        .offset:         48
        .size:           8
        .value_kind:     global_buffer
      - .actual_access:  read_only
        .address_space:  global
        .offset:         56
        .size:           8
        .value_kind:     global_buffer
    .group_segment_fixed_size: 0
    .kernarg_segment_align: 8
    .kernarg_segment_size: 64
    .language:       OpenCL C
    .language_version:
      - 2
      - 0
    .max_flat_workgroup_size: 64
    .name:           _Z5k_aggILi1EEvPKiS1_S1_PKDv4_jPKfS6_PS2_PDF16_
    .private_segment_fixed_size: 0
    .sgpr_count:     48
    .sgpr_spill_count: 0
    .symbol:         _Z5k_aggILi1EEvPKiS1_S1_PKDv4_jPKfS6_PS2_PDF16_.kd
    .uniform_work_group_size: 1
    .uses_dynamic_stack: false
    .vgpr_count:     64
    .vgpr_spill_count: 0
    .wavefront_size: 64
  - .agpr_count:     0
    .args:
      - .actual_access:  read_only
        .address_space:  global
        .offset:         0
        .size:           8
        .value_kind:     global_buffer
      - .actual_access:  read_only
        .address_space:  global
        .offset:         8
        .size:           8
        .value_kind:     global_buffer
      - .actual_access:  read_only
        .address_space:  global
        .offset:         16
        .size:           8
        .value_kind:     global_buffer
      - .actual_access:  read_only
        .address_space:  global
        .offset:         24
        .size:           8
        .value_kind:     global_buffer
      - .actual_access:  read_only
        .address_space:  global
        .offset:         32
        .size:           8
        .value_kind:     global_buffer
      - .actual_access:  read_only
        .address_space:  global
        .offset:         40
        .size:           8
        .value_kind:     global_buffer
      - .actual_access:  read_only
        .address_space:  global
        .offset:         48
        .size:           8
        .value_kind:     global_buffer
      - .actual_access:  write_only
        .address_space:  global
        .offset:         56
        .size:           8
        .value_kind:     global_buffer
    .group_segment_fixed_size: 0
    .kernarg_segment_align: 8
    .kernarg_segment_size: 64
    .language:       OpenCL C
    .language_version:
      - 2
      - 0
    .max_flat_workgroup_size: 64
    .name:           _Z5k_aggILi2EEvPKiS1_S1_PKDv4_jPKfS6_PS2_PDF16_
    .private_segment_fixed_size: 0
    .sgpr_count:     48
    .sgpr_spill_count: 0
    .symbol:         _Z5k_aggILi2EEvPKiS1_S1_PKDv4_jPKfS6_PS2_PDF16_.kd
    .uniform_work_group_size: 1
    .uses_dynamic_stack: false
    .vgpr_count:     64
    .vgpr_spill_count: 0
    .wavefront_size: 64
